# de-serialised prologues: adaLN silu table, P6 router bias preload, P7 token-row gather (24 loads in flight), P8 slot-table rows, EpiMoe2 wait
# speedup vs baseline: 1.0085x; 1.0037x over previous
; #define LAS __attribute__((address_space(3)))
; __device__ __forceinline__ void p0_adaln(const Params& P, LAS unsigned char* lds, int tid, int item) {
;     const int ks = item & 3, nc = item >> 2;
;     LAS float* sc = (LAS float*)lds;
;     LAS float* red = (LAS float*)(lds + 16384);
;     const float* c = P.in[1];
;     for (int i = tid; i < 4096; i += NTHREADS) { const int kl = i >> 3, b = i & 7; const float v = c[b * 2048 + ks * 512 + kl]; sc[i] = v / (1.0f + expf(-v)); }
;     __syncthreads();
;     if (tid < 384) {
;         const int nq = tid % 48, kg = tid / 48;
;         const float* W = P.in[2] + (size_t)(ks * 512 + kg * 64) * NMOD + nc * 192 + nq * 4;
;         f32x4 acc[8];
; #pragma unroll
;         for (int b = 0; b < 8; ++b) acc[b] = (f32x4){0.f, 0.f, 0.f, 0.f};
.LBB0_8:
	s_and_b32 s4, s37, 3
	s_lshl_b32 s4, s4, 9
	v_readlane_b32 s40, v254, 7
	v_add_lshl_u32 v42, v44, s4, 2
	v_readlane_b32 s42, v254, 9
	v_readlane_b32 s43, v254, 10
	s_mov_b64 s[4:5], 0
	v_mov_b32_e32 v4, v72
	v_lshl_add_u64 v[2:3], s[42:43], 0, v[42:43]
	v_mov_b32_e32 v5, v71
	v_readlane_b32 s41, v254, 8
	v_readlane_b32 s44, v254, 11
	v_readlane_b32 s45, v254, 12
	v_readlane_b32 s46, v254, 13
	v_readlane_b32 s47, v254, 14
	v_readlane_b32 s48, v254, 15
	v_readlane_b32 s49, v254, 16
	v_readlane_b32 s50, v254, 17
	v_readlane_b32 s51, v254, 18
	v_readlane_b32 s52, v254, 19
	v_readlane_b32 s53, v254, 20
	v_readlane_b32 s54, v254, 21
	v_readlane_b32 s55, v254, 22
	global_load_dword v100, v[2:3], off
	global_load_dword v101, v[2:3], off offset:256
	global_load_dword v102, v[2:3], off offset:512
	global_load_dword v103, v[2:3], off offset:768
	global_load_dword v104, v[2:3], off offset:1024
	global_load_dword v105, v[2:3], off offset:1280
	global_load_dword v106, v[2:3], off offset:1536
	global_load_dword v107, v[2:3], off offset:1792
	s_waitcnt vmcnt(0)
.LBB0_9:
	v_mov_b32_e32 v6, v100
	s_mov_b64 s[8:9], 0x100
	v_add_u32_e32 v5, 0x200, v5
	v_lshl_add_u64 v[2:3], v[2:3], 0, s[8:9]
	s_movk_i32 s8, 0xdff
	v_cmp_lt_u32_e32 vcc, s8, v5
	s_mov_b32 s8, 0xbfb8aa3b
	s_or_b64 s[4:5], vcc, s[4:5]
	v_mul_f32_e32 v7, 0xbfb8aa3b, v6
	v_rndne_f32_e32 v8, v7
	v_fma_f32 v9, v6, s8, -v7
	v_sub_f32_e32 v7, v7, v8
	v_fmac_f32_e32 v9, 0xb2a5705f, v6
	v_add_f32_e32 v7, v7, v9
	v_cvt_i32_f32_e32 v8, v8
	v_exp_f32_e32 v7, v7
	s_mov_b32 s8, 0x42ce8ed0
	v_cmp_nlt_f32_e32 vcc, s8, v6
	s_mov_b32 s8, 0xc2b17218
	v_ldexp_f32 v7, v7, v8
	v_cndmask_b32_e32 v7, 0, v7, vcc
	v_cmp_ngt_f32_e32 vcc, s8, v6
	s_nop 1
	v_cndmask_b32_e32 v7, v75, v7, vcc
	v_add_f32_e32 v7, 1.0, v7
	v_div_scale_f32 v8, s[8:9], v7, v7, v6
	v_rcp_f32_e32 v9, v8
	v_div_scale_f32 v10, vcc, v6, v7, v6
	v_fma_f32 v11, -v8, v9, 1.0
	v_fmac_f32_e32 v9, v11, v9
	v_mul_f32_e32 v11, v10, v9
	v_fma_f32 v12, -v8, v11, v10
	v_fmac_f32_e32 v11, v12, v9
	v_fma_f32 v8, -v8, v11, v10
	v_div_fmas_f32 v8, v8, v9, v11
	v_div_fixup_f32 v6, v8, v7, v6
	ds_write_b32 v4, v6
	v_add_u32_e32 v4, 0x800, v4
	v_mov_b32_e32 v100, v101
	v_mov_b32_e32 v101, v102
	v_mov_b32_e32 v102, v103
	v_mov_b32_e32 v103, v104
	v_mov_b32_e32 v104, v105
	v_mov_b32_e32 v105, v106
	v_mov_b32_e32 v106, v107
	s_andn2_b64 exec, exec, s[4:5]
	s_cbranch_execnz .LBB0_9
	s_or_b64 exec, exec, s[4:5]
	s_ashr_i32 s4, s38, 2
	s_mulk_i32 s4, 0xc0
	s_waitcnt lgkmcnt(0)
	s_barrier
	s_and_saveexec_b64 s[8:9], s[6:7]
	s_xor_b64 s[8:9], exec, s[8:9]
	s_ashr_i32 s5, s4, 31
	s_or_saveexec_b64 s[8:9], s[8:9]
	s_and_b32 s39, s38, 3
	v_mov_b64_e32 v[2:3], s[4:5]
	s_xor_b64 exec, exec, s[8:9]
	s_cbranch_execz .LBB0_16
	v_lshl_add_u32 v2, s39, 9, v45
	v_mul_u32_u24_e32 v2, 0x3000, v2
	v_readlane_b32 s40, v254, 7
	v_lshlrev_b32_e32 v42, 2, v2
	v_readlane_b32 s44, v254, 11
	v_readlane_b32 s45, v254, 12
	s_ashr_i32 s5, s4, 31
	v_mov_b32_e32 v47, v43
	v_lshl_add_u64 v[2:3], s[44:45], 0, v[42:43]
	v_lshl_add_u64 v[2:3], s[4:5], 2, v[2:3]
	v_lshl_add_u64 v[48:49], v[2:3], 0, v[46:47]
	v_mov_b32_e32 v2, 0
	s_mov_b64 s[10:11], 0
	v_mov_b32_e32 v47, v73
	v_mov_b32_e32 v3, v2
	v_mov_b32_e32 v4, v2
	v_mov_b32_e32 v5, v2
	v_mov_b32_e32 v18, v2
	v_mov_b32_e32 v19, v2
	v_mov_b32_e32 v20, v2
	v_mov_b32_e32 v21, v2
	v_mov_b32_e32 v26, v2
	v_mov_b32_e32 v27, v2
	v_mov_b32_e32 v28, v2
	v_mov_b32_e32 v29, v2
	v_mov_b32_e32 v30, v2
	v_mov_b32_e32 v31, v2
	v_mov_b32_e32 v32, v2
	v_mov_b32_e32 v33, v2
	v_mov_b32_e32 v10, v2
	v_mov_b32_e32 v11, v2
	v_mov_b32_e32 v12, v2
	v_mov_b32_e32 v13, v2
	v_mov_b32_e32 v14, v2
	v_mov_b32_e32 v15, v2
	v_mov_b32_e32 v16, v2
	v_mov_b32_e32 v17, v2
	v_mov_b32_e32 v34, v2
	v_mov_b32_e32 v35, v2
	v_mov_b32_e32 v36, v2
	v_mov_b32_e32 v37, v2
	v_mov_b32_e32 v38, v2
	v_mov_b32_e32 v39, v2
	v_mov_b32_e32 v40, v2
	v_mov_b32_e32 v41, v2
	v_readlane_b32 s41, v254, 8
	v_readlane_b32 s42, v254, 9
	v_readlane_b32 s43, v254, 10
	v_readlane_b32 s46, v254, 13
	v_readlane_b32 s47, v254, 14
	v_readlane_b32 s48, v254, 15
	v_readlane_b32 s49, v254, 16
	v_readlane_b32 s50, v254, 17
	v_readlane_b32 s51, v254, 18
	v_readlane_b32 s52, v254, 19
	v_readlane_b32 s53, v254, 20
	v_readlane_b32 s54, v254, 21
	v_readlane_b32 s55, v254, 22

; __device__ __forceinline__ void p6_route(const Params& P, LAS unsigned char* lds, int tid, int blk, int G) {
;     ...
;         for (int o = tid; o < 64 * 36; o += NTHREADS) { const int r = o / 36, nn = o % 36; float sum = 0.f;
; #pragma unroll
;             for (int w = 0; w < 8; ++w) sum += lg[(w * 64 + r) * 48 + nn];
;             lgr[o] = sum; }
;         __syncthreads();
;         if (tid < 64) {
;             const int tok = rb * 64 + tid;
;             float l[36];
; #pragma unroll
;             for (int nn = 0; nn < 36; ++nn) l[nn] = lgr[tid * 36 + nn];
;             float gl[4]; int gs = 0;
; #pragma unroll
;             for (int j = 0; j < 4; ++j) gl[j] = l[j] + P.in[20][j];
; #pragma unroll
;             for (int j = 1; j < 4; ++j) if (gl[j] > gl[gs]) gs = j;
;             float gmax = gl[0];
; #pragma unroll
;             for (int j = 1; j < 4; ++j) gmax = fmaxf(gmax, gl[j]);
;             float den = 0.f;
; #pragma unroll
;             for (int j = 0; j < 4; ++j) den += expf(gl[j] - gmax);
;             const float gw = 1.0f / den;
;             float el[8];
; #pragma unroll
;             for (int j = 0; j < 8; ++j) { float v = 0.f;
; #pragma unroll
;                 for (int q = 0; q < 4; ++q) v = (gs == q) ? (l[4 + q * 8 + j] + P.in[22][q * 8 + j]) : v;
;                 el[j] = v; }
.LBB0_835:
	v_mul_u32_u24_sdwa v4, v3, s51 dst_sel:DWORD dst_unused:UNUSED_PAD src0_sel:WORD_0 src1_sel:DWORD
	v_lshrrev_b32_e32 v4, 21, v4
	v_mul_lo_u16_e32 v6, 36, v4
	v_add_u32_e32 v5, 0x200, v3
	v_sub_u16_e32 v6, v3, v6
	v_cmp_lt_u32_e32 vcc, s52, v3
	v_mul_u32_u24_e32 v4, 0xc0, v4
	v_mov_b32_e32 v3, v5
	v_lshlrev_b32_e32 v5, 2, v6
	v_add3_u32 v8, 0, v5, v4
	ds_read2st64_b32 v[4:5], v8 offset0:64 offset1:112
	ds_read2st64_b32 v[6:7], v8 offset0:160 offset1:208
	v_add_u32_e32 v9, 0x4000, v8
	v_add_u32_e32 v10, 0x16000, v8
	v_add_u32_e32 v11, 0x19000, v8
	s_waitcnt lgkmcnt(1)
	v_add_f32_e32 v4, 0, v4
	ds_read2st64_b32 v[8:9], v9 offset0:192 offset1:240
	ds_read_b32 v10, v10
	ds_read_b32 v11, v11
	v_add_f32_e32 v4, v4, v5
	s_waitcnt lgkmcnt(3)
	v_add_f32_e32 v4, v4, v6
	v_add_f32_e32 v4, v4, v7
	s_waitcnt lgkmcnt(2)
	v_add_f32_e32 v4, v4, v8
	v_add_f32_e32 v4, v4, v9
	s_waitcnt lgkmcnt(1)
	v_add_f32_e32 v4, v4, v10
	s_waitcnt lgkmcnt(0)
	v_add_f32_e32 v4, v4, v11
	s_or_b64 s[0:1], vcc, s[0:1]
	ds_write_b32 v2, v4
	v_add_u32_e32 v2, 0x800, v2
	s_andn2_b64 exec, exec, s[0:1]
	s_cbranch_execnz .LBB0_835
	s_or_b64 exec, exec, s[0:1]
	s_waitcnt lgkmcnt(0)
	s_barrier
	s_mov_b64 s[36:37], exec
	v_readlane_b32 s0, v254, 2
	v_readlane_b32 s1, v254, 3
	s_and_b64 s[0:1], s[36:37], s[0:1]
	s_mov_b64 exec, s[0:1]
	s_cbranch_execz .LBB0_902
	global_load_dwordx4 v[40:43], v179, s[88:89]
	global_load_dwordx4 v[100:103], v179, s[92:93]
	global_load_dwordx4 v[104:107], v179, s[92:93] offset:16
	global_load_dwordx4 v[108:111], v179, s[92:93] offset:32
	global_load_dwordx4 v[112:115], v179, s[92:93] offset:48
	global_load_dwordx4 v[116:119], v179, s[92:93] offset:64
	global_load_dwordx4 v[120:123], v179, s[92:93] offset:80
	global_load_dwordx4 v[124:127], v179, s[92:93] offset:96
	global_load_dwordx4 v[128:131], v179, s[92:93] offset:112
	v_add_u32_e32 v2, 0, v230
	v_add_u32_e32 v2, 0x1c000, v2
	ds_read2_b32 v[26:27], v2 offset0:7 offset1:8
	ds_read2_b32 v[18:19], v2 offset0:9 offset1:10
	ds_read2_b32 v[10:11], v2 offset0:11 offset1:12
	ds_read2_b32 v[32:33], v2 offset0:13 offset1:14
	ds_read2_b32 v[24:25], v2 offset0:15 offset1:16
	ds_read2_b32 v[16:17], v2 offset0:17 offset1:18
	ds_read2_b32 v[8:9], v2 offset0:19 offset1:20
	ds_read2_b32 v[30:31], v2 offset0:21 offset1:22
	ds_read2_b32 v[34:35], v2 offset0:5 offset1:6
	ds_read_b128 v[44:47], v2
	ds_read2_b32 v[22:23], v2 offset0:23 offset1:24
	ds_read2_b32 v[14:15], v2 offset0:25 offset1:26
	ds_read2_b32 v[6:7], v2 offset0:27 offset1:28
	ds_read2_b32 v[28:29], v2 offset0:29 offset1:30
	ds_read2_b32 v[20:21], v2 offset0:31 offset1:32
	ds_read2_b32 v[12:13], v2 offset0:33 offset1:34
	ds_read_b32 v38, v2 offset:140
	s_waitcnt vmcnt(0) lgkmcnt(7)
	v_pk_add_f32 v[4:5], v[44:45], v[40:41]
	s_nop 0
	v_cmp_gt_f32_e32 vcc, v5, v4
	v_pk_add_f32 v[2:3], v[46:47], v[42:43]
	s_nop 0
	v_cndmask_b32_e32 v37, v4, v5, vcc
	v_cndmask_b32_e64 v36, 0, 1, vcc
	v_cmp_gt_f32_e64 s[0:1], v2, v37
	s_nop 1
	v_cndmask_b32_e64 v36, v36, 2, s[0:1]
	v_cmp_eq_u32_e32 vcc, 1, v36
	s_nop 1
	v_cndmask_b32_e32 v37, v4, v5, vcc
	v_cmp_eq_u32_e32 vcc, 2, v36
	s_nop 1
	v_cndmask_b32_e32 v37, v37, v2, vcc
	v_cmp_eq_u32_e32 vcc, 3, v36
	s_nop 1
	v_cndmask_b32_e32 v37, v37, v3, vcc
	v_cmp_ngt_f32_e64 s[14:15], v3, v37
	v_cmp_gt_f32_e32 vcc, v3, v37
	v_mov_b32_e32 v37, 0
	v_cndmask_b32_e64 v36, 3, v36, s[14:15]
	v_cmp_eq_u32_e64 s[10:11], 0, v36
	s_and_saveexec_b64 s[12:13], s[10:11]
	s_cbranch_execz .LBB0_869
	v_mov_b32_e32 v37, v100
	s_add_i32 s30, 0, 0x1c000
	v_add_u32_e32 v39, s30, v230
	ds_read_b32 v39, v39 offset:16
	s_waitcnt lgkmcnt(0)
	v_add_f32_e32 v37, v39, v37
	s_or_b64 exec, exec, s[12:13]
	v_cmp_eq_u32_e64 s[12:13], 1, v36
	s_and_saveexec_b64 s[38:39], s[12:13]
	s_cbranch_execnz .LBB0_870

; __device__ __forceinline__ void p6_route(const Params& P, LAS unsigned char* lds, int tid, int blk, int G) {
;     ...
;             float el[8];
; #pragma unroll
;             for (int j = 0; j < 8; ++j) { float v = 0.f;
; #pragma unroll
;                 for (int q = 0; q < 4; ++q) v = (gs == q) ? (l[4 + q * 8 + j] + P.in[22][q * 8 + j]) : v;
;                 el[j] = v; }
.LBB0_840:
	v_mov_b32_e32 v11, v116
	s_nop 0
	v_add_f32_e32 v37, v9, v11
	s_or_b64 exec, exec, s[14:15]
	s_and_saveexec_b64 s[14:15], vcc
	s_cbranch_execnz .LBB0_872

; __device__ __forceinline__ void p6_route(const Params& P, LAS unsigned char* lds, int tid, int blk, int G) {
;     ...
;             float el[8];
; #pragma unroll
;             for (int j = 0; j < 8; ++j) { float v = 0.f;
; #pragma unroll
;                 for (int q = 0; q < 4; ++q) v = (gs == q) ? (l[4 + q * 8 + j] + P.in[22][q * 8 + j]) : v;
;                 el[j] = v; }
.LBB0_842:
	v_mov_b32_e32 v7, v101
	s_nop 0
	v_add_f32_e32 v7, v34, v7
	s_or_b64 exec, exec, s[14:15]
	s_and_saveexec_b64 s[14:15], s[12:13]
	s_cbranch_execnz .LBB0_874

; __device__ __forceinline__ void p6_route(const Params& P, LAS unsigned char* lds, int tid, int blk, int G) {
;     ...
;             float el[8];
; #pragma unroll
;             for (int j = 0; j < 8; ++j) { float v = 0.f;
; #pragma unroll
;                 for (int q = 0; q < 4; ++q) v = (gs == q) ? (l[4 + q * 8 + j] + P.in[22][q * 8 + j]) : v;
;                 el[j] = v; }
.LBB0_844:
	v_mov_b32_e32 v7, v117
	s_nop 0
	v_add_f32_e32 v7, v30, v7
	s_or_b64 exec, exec, s[14:15]
	s_and_saveexec_b64 s[14:15], vcc
	s_cbranch_execnz .LBB0_876

; __device__ __forceinline__ void p6_route(const Params& P, LAS unsigned char* lds, int tid, int blk, int G) {
;     ...
;             float el[8];
; #pragma unroll
;             for (int j = 0; j < 8; ++j) { float v = 0.f;
; #pragma unroll
;                 for (int q = 0; q < 4; ++q) v = (gs == q) ? (l[4 + q * 8 + j] + P.in[22][q * 8 + j]) : v;
;                 el[j] = v; }
.LBB0_846:
	v_mov_b32_e32 v9, v102
	s_nop 0
	v_add_f32_e32 v9, v35, v9
	s_or_b64 exec, exec, s[14:15]
	s_and_saveexec_b64 s[14:15], s[12:13]
	s_cbranch_execnz .LBB0_878

; __device__ __forceinline__ void p6_route(const Params& P, LAS unsigned char* lds, int tid, int blk, int G) {
;     ...
;             float el[8];
; #pragma unroll
;             for (int j = 0; j < 8; ++j) { float v = 0.f;
; #pragma unroll
;                 for (int q = 0; q < 4; ++q) v = (gs == q) ? (l[4 + q * 8 + j] + P.in[22][q * 8 + j]) : v;
;                 el[j] = v; }
.LBB0_848:
	v_mov_b32_e32 v9, v118
	s_nop 0
	v_add_f32_e32 v9, v31, v9
	s_or_b64 exec, exec, s[14:15]
	s_and_saveexec_b64 s[14:15], vcc
	s_cbranch_execnz .LBB0_880

; __device__ __forceinline__ void p6_route(const Params& P, LAS unsigned char* lds, int tid, int blk, int G) {
;     ...
;             float el[8];
; #pragma unroll
;             for (int j = 0; j < 8; ++j) { float v = 0.f;
; #pragma unroll
;                 for (int q = 0; q < 4; ++q) v = (gs == q) ? (l[4 + q * 8 + j] + P.in[22][q * 8 + j]) : v;
;                 el[j] = v; }
.LBB0_850:
	v_mov_b32_e32 v11, v103
	s_nop 0
	v_add_f32_e32 v11, v26, v11
	s_or_b64 exec, exec, s[14:15]
	s_and_saveexec_b64 s[14:15], s[12:13]
	s_cbranch_execnz .LBB0_882

; __device__ __forceinline__ void p6_route(const Params& P, LAS unsigned char* lds, int tid, int blk, int G) {
;     ...
;             float el[8];
; #pragma unroll
;             for (int j = 0; j < 8; ++j) { float v = 0.f;
; #pragma unroll
;                 for (int q = 0; q < 4; ++q) v = (gs == q) ? (l[4 + q * 8 + j] + P.in[22][q * 8 + j]) : v;
;                 el[j] = v; }
.LBB0_852:
	v_mov_b32_e32 v11, v119
	s_nop 0
	v_add_f32_e32 v11, v22, v11
	s_or_b64 exec, exec, s[14:15]
	s_and_saveexec_b64 s[14:15], vcc
	s_cbranch_execnz .LBB0_884

; __device__ __forceinline__ void p6_route(const Params& P, LAS unsigned char* lds, int tid, int blk, int G) {
;     ...
;             float el[8];
; #pragma unroll
;             for (int j = 0; j < 8; ++j) { float v = 0.f;
; #pragma unroll
;                 for (int q = 0; q < 4; ++q) v = (gs == q) ? (l[4 + q * 8 + j] + P.in[22][q * 8 + j]) : v;
;                 el[j] = v; }
.LBB0_854:
	v_mov_b32_e32 v20, v104
	s_nop 0
	v_add_f32_e32 v20, v27, v20
	s_or_b64 exec, exec, s[14:15]
	s_and_saveexec_b64 s[14:15], s[12:13]
	s_cbranch_execnz .LBB0_886

; __device__ __forceinline__ void p6_route(const Params& P, LAS unsigned char* lds, int tid, int blk, int G) {
;     ...
;             float el[8];
; #pragma unroll
;             for (int j = 0; j < 8; ++j) { float v = 0.f;
; #pragma unroll
;                 for (int q = 0; q < 4; ++q) v = (gs == q) ? (l[4 + q * 8 + j] + P.in[22][q * 8 + j]) : v;
;                 el[j] = v; }
.LBB0_856:
	v_mov_b32_e32 v20, v120
	s_nop 0
	v_add_f32_e32 v20, v23, v20
	s_or_b64 exec, exec, s[14:15]
	s_and_saveexec_b64 s[14:15], vcc
	s_cbranch_execnz .LBB0_888

; __device__ __forceinline__ void p6_route(const Params& P, LAS unsigned char* lds, int tid, int blk, int G) {
;     ...
;             float el[8];
; #pragma unroll
;             for (int j = 0; j < 8; ++j) { float v = 0.f;
; #pragma unroll
;                 for (int q = 0; q < 4; ++q) v = (gs == q) ? (l[4 + q * 8 + j] + P.in[22][q * 8 + j]) : v;
;                 el[j] = v; }
.LBB0_858:
	v_mov_b32_e32 v21, v105
	s_nop 0
	v_add_f32_e32 v21, v18, v21
	s_or_b64 exec, exec, s[14:15]
	s_and_saveexec_b64 s[14:15], s[12:13]
	s_cbranch_execnz .LBB0_890

; __device__ __forceinline__ void p6_route(const Params& P, LAS unsigned char* lds, int tid, int blk, int G) {
;     ...
;             float el[8];
; #pragma unroll
;             for (int j = 0; j < 8; ++j) { float v = 0.f;
; #pragma unroll
;                 for (int q = 0; q < 4; ++q) v = (gs == q) ? (l[4 + q * 8 + j] + P.in[22][q * 8 + j]) : v;
;                 el[j] = v; }
.LBB0_860:
	v_mov_b32_e32 v16, v121
	s_nop 0
	v_add_f32_e32 v21, v14, v16
	s_or_b64 exec, exec, s[14:15]
	s_and_saveexec_b64 s[14:15], vcc
	s_cbranch_execnz .LBB0_892

; __device__ __forceinline__ void p6_route(const Params& P, LAS unsigned char* lds, int tid, int blk, int G) {
;     ...
;             float el[8];
; #pragma unroll
;             for (int j = 0; j < 8; ++j) { float v = 0.f;
; #pragma unroll
;                 for (int q = 0; q < 4; ++q) v = (gs == q) ? (l[4 + q * 8 + j] + P.in[22][q * 8 + j]) : v;
;                 el[j] = v; }
.LBB0_862:
	v_mov_b32_e32 v12, v106
	s_nop 0
	v_add_f32_e32 v12, v19, v12
	s_or_b64 exec, exec, s[14:15]
	s_and_saveexec_b64 s[14:15], s[12:13]
	s_cbranch_execnz .LBB0_894

; __device__ __forceinline__ void p6_route(const Params& P, LAS unsigned char* lds, int tid, int blk, int G) {
;     ...
;             float el[8];
; #pragma unroll
;             for (int j = 0; j < 8; ++j) { float v = 0.f;
; #pragma unroll
;                 for (int q = 0; q < 4; ++q) v = (gs == q) ? (l[4 + q * 8 + j] + P.in[22][q * 8 + j]) : v;
;                 el[j] = v; }
.LBB0_864:
	v_mov_b32_e32 v12, v122
	s_nop 0
	v_add_f32_e32 v12, v15, v12
	s_or_b64 exec, exec, s[14:15]
	s_and_saveexec_b64 s[14:15], vcc
	s_cbranch_execnz .LBB0_896

; __device__ __forceinline__ void p6_route(const Params& P, LAS unsigned char* lds, int tid, int blk, int G) {
;     ...
;             float el[8];
; #pragma unroll
;             for (int j = 0; j < 8; ++j) { float v = 0.f;
; #pragma unroll
;                 for (int q = 0; q < 4; ++q) v = (gs == q) ? (l[4 + q * 8 + j] + P.in[22][q * 8 + j]) : v;
;                 el[j] = v; }
.LBB0_866:
	v_mov_b32_e32 v13, v107
	s_nop 0
	v_add_f32_e32 v13, v10, v13
	s_or_b64 exec, exec, s[14:15]
	s_and_saveexec_b64 s[10:11], s[12:13]
	s_cbranch_execnz .LBB0_898

; __device__ __forceinline__ void p6_route(const Params& P, LAS unsigned char* lds, int tid, int blk, int G) {
;     ...
;             float el[8];
; #pragma unroll
;             for (int j = 0; j < 8; ++j) { float v = 0.f;
; #pragma unroll
;                 for (int q = 0; q < 4; ++q) v = (gs == q) ? (l[4 + q * 8 + j] + P.in[22][q * 8 + j]) : v;
;                 el[j] = v; }
.LBB0_868:
	v_mov_b32_e32 v8, v123
	s_nop 0
	v_add_f32_e32 v13, v6, v8
	s_or_b64 exec, exec, s[10:11]
	s_and_saveexec_b64 s[0:1], vcc
	s_cbranch_execnz .LBB0_900
	s_branch .LBB0_901

; __device__ __forceinline__ void p6_route(const Params& P, LAS unsigned char* lds, int tid, int blk, int G) {
;     ...
;             float el[8];
; #pragma unroll
;             for (int j = 0; j < 8; ++j) { float v = 0.f;
; #pragma unroll
;                 for (int q = 0; q < 4; ++q) v = (gs == q) ? (l[4 + q * 8 + j] + P.in[22][q * 8 + j]) : v;
;                 el[j] = v; }
.LBB0_870:
	v_mov_b32_e32 v37, v108
	s_nop 0
	v_add_f32_e32 v37, v11, v37
	s_or_b64 exec, exec, s[38:39]
	s_and_b64 s[0:1], s[0:1], s[14:15]
	s_and_saveexec_b64 s[14:15], s[0:1]
	s_cbranch_execnz .LBB0_840

; __device__ __forceinline__ void p6_route(const Params& P, LAS unsigned char* lds, int tid, int blk, int G) {
;     ...
;             float el[8];
; #pragma unroll
;             for (int j = 0; j < 8; ++j) { float v = 0.f;
; #pragma unroll
;                 for (int q = 0; q < 4; ++q) v = (gs == q) ? (l[4 + q * 8 + j] + P.in[22][q * 8 + j]) : v;
;                 el[j] = v; }
.LBB0_872:
	v_mov_b32_e32 v9, v124
	s_waitcnt lgkmcnt(4)
	v_add_f32_e32 v37, v7, v9
	s_or_b64 exec, exec, s[14:15]
	v_mov_b32_e32 v7, 0
	s_and_saveexec_b64 s[14:15], s[10:11]
	s_cbranch_execnz .LBB0_842

; __device__ __forceinline__ void p6_route(const Params& P, LAS unsigned char* lds, int tid, int blk, int G) {
;     ...
;             float el[8];
; #pragma unroll
;             for (int j = 0; j < 8; ++j) { float v = 0.f;
; #pragma unroll
;                 for (int q = 0; q < 4; ++q) v = (gs == q) ? (l[4 + q * 8 + j] + P.in[22][q * 8 + j]) : v;
;                 el[j] = v; }
.LBB0_874:
	v_mov_b32_e32 v7, v109
	s_nop 0
	v_add_f32_e32 v7, v32, v7
	s_or_b64 exec, exec, s[14:15]
	s_and_saveexec_b64 s[14:15], s[0:1]
	s_cbranch_execnz .LBB0_844

; __device__ __forceinline__ void p6_route(const Params& P, LAS unsigned char* lds, int tid, int blk, int G) {
;     ...
;             float el[8];
; #pragma unroll
;             for (int j = 0; j < 8; ++j) { float v = 0.f;
; #pragma unroll
;                 for (int q = 0; q < 4; ++q) v = (gs == q) ? (l[4 + q * 8 + j] + P.in[22][q * 8 + j]) : v;
;                 el[j] = v; }
.LBB0_876:
	v_mov_b32_e32 v7, v125
	s_waitcnt lgkmcnt(3)
	v_add_f32_e32 v7, v28, v7
	s_or_b64 exec, exec, s[14:15]
	v_mov_b32_e32 v9, 0
	s_and_saveexec_b64 s[14:15], s[10:11]
	s_cbranch_execnz .LBB0_846

; __device__ __forceinline__ void p6_route(const Params& P, LAS unsigned char* lds, int tid, int blk, int G) {
;     ...
;             float el[8];
; #pragma unroll
;             for (int j = 0; j < 8; ++j) { float v = 0.f;
; #pragma unroll
;                 for (int q = 0; q < 4; ++q) v = (gs == q) ? (l[4 + q * 8 + j] + P.in[22][q * 8 + j]) : v;
;                 el[j] = v; }
.LBB0_878:
	v_mov_b32_e32 v9, v110
	s_nop 0
	v_add_f32_e32 v9, v33, v9
	s_or_b64 exec, exec, s[14:15]
	s_and_saveexec_b64 s[14:15], s[0:1]
	s_cbranch_execnz .LBB0_848

; __device__ __forceinline__ void p6_route(const Params& P, LAS unsigned char* lds, int tid, int blk, int G) {
;     ...
;             float el[8];
; #pragma unroll
;             for (int j = 0; j < 8; ++j) { float v = 0.f;
; #pragma unroll
;                 for (int q = 0; q < 4; ++q) v = (gs == q) ? (l[4 + q * 8 + j] + P.in[22][q * 8 + j]) : v;
;                 el[j] = v; }
.LBB0_880:
	v_mov_b32_e32 v9, v126
	s_waitcnt lgkmcnt(3)
	v_add_f32_e32 v9, v29, v9
	s_or_b64 exec, exec, s[14:15]
	v_mov_b32_e32 v11, 0
	s_and_saveexec_b64 s[14:15], s[10:11]
	s_cbranch_execnz .LBB0_850

; __device__ __forceinline__ void p6_route(const Params& P, LAS unsigned char* lds, int tid, int blk, int G) {
;     ...
;             float el[8];
; #pragma unroll
;             for (int j = 0; j < 8; ++j) { float v = 0.f;
; #pragma unroll
;                 for (int q = 0; q < 4; ++q) v = (gs == q) ? (l[4 + q * 8 + j] + P.in[22][q * 8 + j]) : v;
;                 el[j] = v; }
.LBB0_882:
	v_mov_b32_e32 v11, v111
	s_nop 0
	v_add_f32_e32 v11, v24, v11
	s_or_b64 exec, exec, s[14:15]
	s_and_saveexec_b64 s[14:15], s[0:1]
	s_cbranch_execnz .LBB0_852

; __device__ __forceinline__ void p6_route(const Params& P, LAS unsigned char* lds, int tid, int blk, int G) {
;     ...
;             float el[8];
; #pragma unroll
;             for (int j = 0; j < 8; ++j) { float v = 0.f;
; #pragma unroll
;                 for (int q = 0; q < 4; ++q) v = (gs == q) ? (l[4 + q * 8 + j] + P.in[22][q * 8 + j]) : v;
;                 el[j] = v; }
.LBB0_884:
	v_mov_b32_e32 v11, v127
	s_waitcnt lgkmcnt(2)
	v_add_f32_e32 v11, v20, v11
	s_or_b64 exec, exec, s[14:15]
	v_mov_b32_e32 v20, 0
	s_and_saveexec_b64 s[14:15], s[10:11]
	s_cbranch_execnz .LBB0_854

; __device__ __forceinline__ void p6_route(const Params& P, LAS unsigned char* lds, int tid, int blk, int G) {
;     ...
;             float el[8];
; #pragma unroll
;             for (int j = 0; j < 8; ++j) { float v = 0.f;
; #pragma unroll
;                 for (int q = 0; q < 4; ++q) v = (gs == q) ? (l[4 + q * 8 + j] + P.in[22][q * 8 + j]) : v;
;                 el[j] = v; }
.LBB0_886:
	v_mov_b32_e32 v20, v112
	s_nop 0
	v_add_f32_e32 v20, v25, v20
	s_or_b64 exec, exec, s[14:15]
	s_and_saveexec_b64 s[14:15], s[0:1]
	s_cbranch_execnz .LBB0_856

; __device__ __forceinline__ void p6_route(const Params& P, LAS unsigned char* lds, int tid, int blk, int G) {
;     ...
;             float el[8];
; #pragma unroll
;             for (int j = 0; j < 8; ++j) { float v = 0.f;
; #pragma unroll
;                 for (int q = 0; q < 4; ++q) v = (gs == q) ? (l[4 + q * 8 + j] + P.in[22][q * 8 + j]) : v;
;                 el[j] = v; }
.LBB0_888:
	v_mov_b32_e32 v20, v128
	s_nop 0
	v_add_f32_e32 v20, v21, v20
	s_or_b64 exec, exec, s[14:15]
	v_mov_b32_e32 v21, 0
	s_and_saveexec_b64 s[14:15], s[10:11]
	s_cbranch_execnz .LBB0_858

; __device__ __forceinline__ void p6_route(const Params& P, LAS unsigned char* lds, int tid, int blk, int G) {
;     ...
;             float el[8];
; #pragma unroll
;             for (int j = 0; j < 8; ++j) { float v = 0.f;
; #pragma unroll
;                 for (int q = 0; q < 4; ++q) v = (gs == q) ? (l[4 + q * 8 + j] + P.in[22][q * 8 + j]) : v;
;                 el[j] = v; }
.LBB0_890:
	v_mov_b32_e32 v18, v113
	s_nop 0
	v_add_f32_e32 v21, v16, v18
	s_or_b64 exec, exec, s[14:15]
	s_and_saveexec_b64 s[14:15], s[0:1]
	s_cbranch_execnz .LBB0_860

; __device__ __forceinline__ void p6_route(const Params& P, LAS unsigned char* lds, int tid, int blk, int G) {
;     ...
;             float el[8];
; #pragma unroll
;             for (int j = 0; j < 8; ++j) { float v = 0.f;
; #pragma unroll
;                 for (int q = 0; q < 4; ++q) v = (gs == q) ? (l[4 + q * 8 + j] + P.in[22][q * 8 + j]) : v;
;                 el[j] = v; }
.LBB0_892:
	v_mov_b32_e32 v14, v129
	s_waitcnt lgkmcnt(1)
	v_add_f32_e32 v21, v12, v14
	s_or_b64 exec, exec, s[14:15]
	v_mov_b32_e32 v12, 0
	s_and_saveexec_b64 s[14:15], s[10:11]
	s_cbranch_execnz .LBB0_862

; __device__ __forceinline__ void p6_route(const Params& P, LAS unsigned char* lds, int tid, int blk, int G) {
;     ...
;             float el[8];
; #pragma unroll
;             for (int j = 0; j < 8; ++j) { float v = 0.f;
; #pragma unroll
;                 for (int q = 0; q < 4; ++q) v = (gs == q) ? (l[4 + q * 8 + j] + P.in[22][q * 8 + j]) : v;
;                 el[j] = v; }
.LBB0_894:
	v_mov_b32_e32 v12, v114
	s_nop 0
	v_add_f32_e32 v12, v17, v12
	s_or_b64 exec, exec, s[14:15]
	s_and_saveexec_b64 s[14:15], s[0:1]
	s_cbranch_execnz .LBB0_864

; __device__ __forceinline__ void p6_route(const Params& P, LAS unsigned char* lds, int tid, int blk, int G) {
;     ...
;             float el[8];
; #pragma unroll
;             for (int j = 0; j < 8; ++j) { float v = 0.f;
; #pragma unroll
;                 for (int q = 0; q < 4; ++q) v = (gs == q) ? (l[4 + q * 8 + j] + P.in[22][q * 8 + j]) : v;
;                 el[j] = v; }
.LBB0_896:
	v_mov_b32_e32 v12, v130
	s_nop 0
	v_add_f32_e32 v12, v13, v12
	s_or_b64 exec, exec, s[14:15]
	v_mov_b32_e32 v13, 0
	s_and_saveexec_b64 s[14:15], s[10:11]
	s_cbranch_execnz .LBB0_866

; __device__ __forceinline__ void p6_route(const Params& P, LAS unsigned char* lds, int tid, int blk, int G) {
;     ...
;             float el[8];
; #pragma unroll
;             for (int j = 0; j < 8; ++j) { float v = 0.f;
; #pragma unroll
;                 for (int q = 0; q < 4; ++q) v = (gs == q) ? (l[4 + q * 8 + j] + P.in[22][q * 8 + j]) : v;
;                 el[j] = v; }
.LBB0_898:
	v_mov_b32_e32 v10, v115
	s_nop 0
	v_add_f32_e32 v13, v8, v10
	s_or_b64 exec, exec, s[10:11]
	s_and_saveexec_b64 s[10:11], s[0:1]
	s_cbranch_execnz .LBB0_868

; __device__ __forceinline__ void p6_route(const Params& P, LAS unsigned char* lds, int tid, int blk, int G) {
;     ...
;             float el[8];
; #pragma unroll
;             for (int j = 0; j < 8; ++j) { float v = 0.f;
; #pragma unroll
;                 for (int q = 0; q < 4; ++q) v = (gs == q) ? (l[4 + q * 8 + j] + P.in[22][q * 8 + j]) : v;
;                 el[j] = v; }
.LBB0_900:
	v_mov_b32_e32 v6, v131
	s_waitcnt lgkmcnt(0)
	v_add_f32_e32 v13, v38, v6

; __global__ void __launch_bounds__(NTHREADS, 2) hymba_fwd(Params P) {
;     ...
;             { int R0, C0, R1, C1; g8::stage_rc(tid * 16, R0, C0); g8::stage_rc(tid * 16 + 8192, R1, C1);
; #pragma unroll
;               for (int k = 0; k < 6; ++k) { g8::Unit uk; uk.aux = 0; uk.aux2 = 0; const bool ok = S.next(k, uk);
;                   const int e = uk.aux & 255, r0 = uk.aux >> 8, n = ok ? uk.aux2 : 0; const int* le = (const int*)(ws + WS_LIST) + (ok ? e * 16384 + r0 : 0);
;                   const unsigned a0 = (R0 < n) ? (unsigned)(le[R0] >> 1) : 0u, a1 = (R1 < n) ? (unsigned)(le[R1] >> 1) : 0u, a2 = (128 + R0 < n) ? (unsigned)(le[128 + R0] >> 1) : 0u, a3 = (128 + R1 < n) ? (unsigned)(le[128 + R1] >> 1) : 0u;
;                   tokt[k * 512 + tid] = (u32x2){a0 | (a1 << 16), a2 | (a3 << 16)}; }
.LBB0_1044:
	v_mov_b32_e32 v105, 0
	v_mov_b32_e32 v106, 0
	v_mov_b32_e32 v107, 0
	v_mov_b32_e32 v108, 0
	v_mov_b32_e32 v109, 0
	v_mov_b32_e32 v110, 0
	v_mov_b32_e32 v111, 0
	v_mov_b32_e32 v112, 0
	v_mov_b32_e32 v113, 0
	v_mov_b32_e32 v114, 0
	v_mov_b32_e32 v115, 0
	v_mov_b32_e32 v116, 0
	v_mov_b32_e32 v117, 0
	v_mov_b32_e32 v118, 0
	v_mov_b32_e32 v119, 0
	v_mov_b32_e32 v120, 0
	v_mov_b32_e32 v121, 0
	v_mov_b32_e32 v122, 0
	v_mov_b32_e32 v123, 0
	v_mov_b32_e32 v124, 0
	v_mov_b32_e32 v125, 0
	v_mov_b32_e32 v126, 0
	v_mov_b32_e32 v127, 0
	v_mov_b32_e32 v128, 0
	s_ashr_i32 s6, s7, 8
	s_lshl_b32 s7, s7, 14
	s_and_b32 s7, s7, 0x3fc000
	s_add_i32 s7, s7, s6
	s_and_b64 s[4:5], s[4:5], exec
	s_cselect_b32 s4, s7, 0
	s_ashr_i32 s5, s4, 31
	v_lshrrev_b32_e32 v2, 3, v0
	v_bfe_u32 v5, v0, 2, 4
	s_lshl_b64 s[4:5], s[4:5], 2
	v_and_or_b32 v198, v2, 48, v5
	s_add_u32 s4, s10, s4
	v_mov_b32_e32 v1, 0
	s_addc_u32 s5, s11, s5
	v_cmp_gt_i32_e32 vcc, s8, v198
	v_mov_b32_e32 v4, 0
	v_lshlrev_b32_e32 v199, 2, v198
	s_and_saveexec_b64 s[6:7], vcc
	s_cbranch_execz .LBB0_1046
	global_load_dword v105, v199, s[4:5]
.LBB0_1046:
	s_or_b64 exec, exec, s[6:7]
	v_bfe_u32 v3, v0, 3, 25
	v_or_b32_e32 v3, 64, v3
	s_movk_i32 s6, 0x70
	v_and_or_b32 v200, v3, s6, v5
	v_cmp_gt_i32_e32 vcc, s8, v200
	v_lshlrev_b32_e32 v201, 2, v200
	s_and_saveexec_b64 s[6:7], vcc
	s_cbranch_execz .LBB0_1048
	global_load_dword v106, v201, s[4:5]
.LBB0_1048:
	s_or_b64 exec, exec, s[6:7]
	v_or_b32_e32 v202, 0x80, v198
	v_cmp_gt_i32_e32 vcc, s8, v202
	v_mov_b32_e32 v6, 0
	v_mov_b32_e32 v5, 0
	s_and_saveexec_b64 s[6:7], vcc
	s_cbranch_execz .LBB0_1050
	global_load_dword v107, v199, s[4:5] offset:512
.LBB0_1050:
	s_or_b64 exec, exec, s[6:7]
	v_or_b32_e32 v203, 0x80, v200
	v_cmp_gt_i32_e32 vcc, s8, v203
	s_and_saveexec_b64 s[6:7], vcc
	s_cbranch_execz .LBB0_1052
	global_load_dword v108, v201, s[4:5] offset:512
.LBB0_1052:
	s_or_b64 exec, exec, s[6:7]
	v_lshl_add_u32 v7, v0, 3, 0
	v_cndmask_b32_e64 v1, 0, 1, s[12:13]
	v_add_u32_e32 v204, 0x20000, v7
	v_cmp_ne_u32_e64 s[4:5], 1, v1
	s_andn2_b64 vcc, exec, s[12:13]
	s_cbranch_vccnz .LBB0_1054
	s_add_i32 s6, s33, s2
	s_ashr_i32 s8, s6, 3
	s_cbranch_execz .LBB0_1055
	s_branch .LBB0_1056

; __global__ void __launch_bounds__(NTHREADS, 2) hymba_fwd(Params P) {
;     ...
;             { int R0, C0, R1, C1; g8::stage_rc(tid * 16, R0, C0); g8::stage_rc(tid * 16 + 8192, R1, C1);
; #pragma unroll
;               for (int k = 0; k < 6; ++k) { g8::Unit uk; uk.aux = 0; uk.aux2 = 0; const bool ok = S.next(k, uk);
;                   const int e = uk.aux & 255, r0 = uk.aux >> 8, n = ok ? uk.aux2 : 0; const int* le = (const int*)(ws + WS_LIST) + (ok ? e * 16384 + r0 : 0);
;                   const unsigned a0 = (R0 < n) ? (unsigned)(le[R0] >> 1) : 0u, a1 = (R1 < n) ? (unsigned)(le[R1] >> 1) : 0u, a2 = (128 + R0 < n) ? (unsigned)(le[128 + R0] >> 1) : 0u, a3 = (128 + R1 < n) ? (unsigned)(le[128 + R1] >> 1) : 0u;
;                   tokt[k * 512 + tid] = (u32x2){a0 | (a1 << 16), a2 | (a3 << 16)}; }
.LBB0_1058:
	s_ashr_i32 s8, s9, 8
	s_lshl_b32 s9, s9, 14
	s_and_b32 s9, s9, 0x3fc000
	s_add_i32 s9, s9, s8
	s_and_b64 s[6:7], s[6:7], exec
	s_cselect_b32 s6, s9, 0
	s_ashr_i32 s7, s6, 31
	s_lshl_b64 s[6:7], s[6:7], 2
	s_add_u32 s6, s10, s6
	s_addc_u32 s7, s11, s7
	v_cmp_gt_i32_e32 vcc, s14, v198
	v_mov_b32_e32 v1, 0
	v_mov_b32_e32 v4, 0
	s_and_saveexec_b64 s[8:9], vcc
	s_cbranch_execz .LBB0_1060
	global_load_dword v109, v199, s[6:7]
.LBB0_1060:
	s_or_b64 exec, exec, s[8:9]
	v_cmp_gt_i32_e32 vcc, s14, v200
	v_mov_b32_e32 v5, 0
	s_and_saveexec_b64 s[8:9], vcc
	s_cbranch_execz .LBB0_1062
	global_load_dword v110, v201, s[6:7]
.LBB0_1062:
	s_or_b64 exec, exec, s[8:9]
	v_cmp_gt_i32_e32 vcc, s14, v202
	s_and_saveexec_b64 s[8:9], vcc
	s_cbranch_execz .LBB0_1064
	global_load_dword v111, v199, s[6:7] offset:512
.LBB0_1064:
	s_or_b64 exec, exec, s[8:9]
	v_cmp_gt_i32_e32 vcc, s14, v203
	v_mov_b32_e32 v6, 0
	s_and_saveexec_b64 s[8:9], vcc
	s_cbranch_execz .LBB0_1066
	global_load_dword v112, v201, s[6:7] offset:512
.LBB0_1066:
	s_or_b64 exec, exec, s[8:9]
	s_and_b64 vcc, exec, s[4:5]
	s_cbranch_vccnz .LBB0_1068
	s_lshl_b32 s6, s33, 1
	s_add_i32 s6, s6, s2
	s_ashr_i32 s8, s6, 3
	s_cbranch_execz .LBB0_1069
	s_branch .LBB0_1070

; __global__ void __launch_bounds__(NTHREADS, 2) hymba_fwd(Params P) {
;     ...
;             { int R0, C0, R1, C1; g8::stage_rc(tid * 16, R0, C0); g8::stage_rc(tid * 16 + 8192, R1, C1);
; #pragma unroll
;               for (int k = 0; k < 6; ++k) { g8::Unit uk; uk.aux = 0; uk.aux2 = 0; const bool ok = S.next(k, uk);
;                   const int e = uk.aux & 255, r0 = uk.aux >> 8, n = ok ? uk.aux2 : 0; const int* le = (const int*)(ws + WS_LIST) + (ok ? e * 16384 + r0 : 0);
;                   const unsigned a0 = (R0 < n) ? (unsigned)(le[R0] >> 1) : 0u, a1 = (R1 < n) ? (unsigned)(le[R1] >> 1) : 0u, a2 = (128 + R0 < n) ? (unsigned)(le[128 + R0] >> 1) : 0u, a3 = (128 + R1 < n) ? (unsigned)(le[128 + R1] >> 1) : 0u;
;                   tokt[k * 512 + tid] = (u32x2){a0 | (a1 << 16), a2 | (a3 << 16)}; }
.LBB0_1072:
	s_ashr_i32 s8, s9, 8
	s_lshl_b32 s9, s9, 14
	s_and_b32 s9, s9, 0x3fc000
	s_add_i32 s9, s9, s8
	s_and_b64 s[6:7], s[6:7], exec
	s_cselect_b32 s6, s9, 0
	s_ashr_i32 s7, s6, 31
	s_lshl_b64 s[6:7], s[6:7], 2
	s_add_u32 s6, s10, s6
	s_addc_u32 s7, s11, s7
	v_cmp_gt_i32_e32 vcc, s14, v198
	v_mov_b32_e32 v1, 0
	v_mov_b32_e32 v4, 0
	s_and_saveexec_b64 s[8:9], vcc
	s_cbranch_execz .LBB0_1074
	global_load_dword v113, v199, s[6:7]
.LBB0_1074:
	s_or_b64 exec, exec, s[8:9]
	v_cmp_gt_i32_e32 vcc, s14, v200
	v_mov_b32_e32 v5, 0
	s_and_saveexec_b64 s[8:9], vcc
	s_cbranch_execz .LBB0_1076
	global_load_dword v114, v201, s[6:7]
.LBB0_1076:
	s_or_b64 exec, exec, s[8:9]
	v_cmp_gt_i32_e32 vcc, s14, v202
	s_and_saveexec_b64 s[8:9], vcc
	s_cbranch_execz .LBB0_1078
	global_load_dword v115, v199, s[6:7] offset:512
.LBB0_1078:
	s_or_b64 exec, exec, s[8:9]
	v_cmp_gt_i32_e32 vcc, s14, v203
	v_mov_b32_e32 v6, 0
	s_and_saveexec_b64 s[8:9], vcc
	s_cbranch_execz .LBB0_1080
	global_load_dword v116, v201, s[6:7] offset:512
.LBB0_1080:
	s_or_b64 exec, exec, s[8:9]
	s_and_b64 vcc, exec, s[4:5]
	s_cbranch_vccnz .LBB0_1082
	s_mul_i32 s6, s33, 3
	s_add_i32 s6, s6, s2
	s_ashr_i32 s8, s6, 3
	s_cbranch_execz .LBB0_1083
	s_branch .LBB0_1084

; __global__ void __launch_bounds__(NTHREADS, 2) hymba_fwd(Params P) {
;     ...
;             { int R0, C0, R1, C1; g8::stage_rc(tid * 16, R0, C0); g8::stage_rc(tid * 16 + 8192, R1, C1);
; #pragma unroll
;               for (int k = 0; k < 6; ++k) { g8::Unit uk; uk.aux = 0; uk.aux2 = 0; const bool ok = S.next(k, uk);
;                   const int e = uk.aux & 255, r0 = uk.aux >> 8, n = ok ? uk.aux2 : 0; const int* le = (const int*)(ws + WS_LIST) + (ok ? e * 16384 + r0 : 0);
;                   const unsigned a0 = (R0 < n) ? (unsigned)(le[R0] >> 1) : 0u, a1 = (R1 < n) ? (unsigned)(le[R1] >> 1) : 0u, a2 = (128 + R0 < n) ? (unsigned)(le[128 + R0] >> 1) : 0u, a3 = (128 + R1 < n) ? (unsigned)(le[128 + R1] >> 1) : 0u;
;                   tokt[k * 512 + tid] = (u32x2){a0 | (a1 << 16), a2 | (a3 << 16)}; }
.LBB0_1086:
	s_ashr_i32 s8, s9, 8
	s_lshl_b32 s9, s9, 14
	s_and_b32 s9, s9, 0x3fc000
	s_add_i32 s9, s9, s8
	s_and_b64 s[6:7], s[6:7], exec
	s_cselect_b32 s6, s9, 0
	s_ashr_i32 s7, s6, 31
	s_lshl_b64 s[6:7], s[6:7], 2
	s_add_u32 s6, s10, s6
	s_addc_u32 s7, s11, s7
	v_cmp_gt_i32_e32 vcc, s14, v198
	v_mov_b32_e32 v1, 0
	v_mov_b32_e32 v4, 0
	s_and_saveexec_b64 s[8:9], vcc
	s_cbranch_execz .LBB0_1088
	global_load_dword v117, v199, s[6:7]
.LBB0_1088:
	s_or_b64 exec, exec, s[8:9]
	v_cmp_gt_i32_e32 vcc, s14, v200
	v_mov_b32_e32 v5, 0
	s_and_saveexec_b64 s[8:9], vcc
	s_cbranch_execz .LBB0_1090
	global_load_dword v118, v201, s[6:7]
.LBB0_1090:
	s_or_b64 exec, exec, s[8:9]
	v_cmp_gt_i32_e32 vcc, s14, v202
	s_and_saveexec_b64 s[8:9], vcc
	s_cbranch_execz .LBB0_1092
	global_load_dword v119, v199, s[6:7] offset:512
.LBB0_1092:
	s_or_b64 exec, exec, s[8:9]
	v_cmp_gt_i32_e32 vcc, s14, v203
	v_mov_b32_e32 v6, 0
	s_and_saveexec_b64 s[8:9], vcc
	s_cbranch_execz .LBB0_1094
	global_load_dword v120, v201, s[6:7] offset:512
.LBB0_1094:
	s_or_b64 exec, exec, s[8:9]
	s_and_b64 vcc, exec, s[4:5]
	s_cbranch_vccnz .LBB0_1096
	s_lshl_b32 s6, s33, 2
	s_add_i32 s6, s6, s2
	s_ashr_i32 s8, s6, 3
	s_cbranch_execz .LBB0_1097
	s_branch .LBB0_1098

; __global__ void __launch_bounds__(NTHREADS, 2) hymba_fwd(Params P) {
;     ...
;             { int R0, C0, R1, C1; g8::stage_rc(tid * 16, R0, C0); g8::stage_rc(tid * 16 + 8192, R1, C1);
; #pragma unroll
;               for (int k = 0; k < 6; ++k) { g8::Unit uk; uk.aux = 0; uk.aux2 = 0; const bool ok = S.next(k, uk);
;                   const int e = uk.aux & 255, r0 = uk.aux >> 8, n = ok ? uk.aux2 : 0; const int* le = (const int*)(ws + WS_LIST) + (ok ? e * 16384 + r0 : 0);
;                   const unsigned a0 = (R0 < n) ? (unsigned)(le[R0] >> 1) : 0u, a1 = (R1 < n) ? (unsigned)(le[R1] >> 1) : 0u, a2 = (128 + R0 < n) ? (unsigned)(le[128 + R0] >> 1) : 0u, a3 = (128 + R1 < n) ? (unsigned)(le[128 + R1] >> 1) : 0u;
;                   tokt[k * 512 + tid] = (u32x2){a0 | (a1 << 16), a2 | (a3 << 16)}; }
.LBB0_1100:
	s_ashr_i32 s8, s9, 8
	s_lshl_b32 s9, s9, 14
	s_and_b32 s9, s9, 0x3fc000
	s_add_i32 s9, s9, s8
	s_and_b64 s[6:7], s[6:7], exec
	s_cselect_b32 s6, s9, 0
	s_ashr_i32 s7, s6, 31
	s_lshl_b64 s[6:7], s[6:7], 2
	s_add_u32 s6, s10, s6
	s_addc_u32 s7, s11, s7
	v_cmp_gt_i32_e32 vcc, s14, v198
	v_mov_b32_e32 v1, 0
	v_mov_b32_e32 v4, 0
	s_and_saveexec_b64 s[8:9], vcc
	s_cbranch_execz .LBB0_1102
	global_load_dword v121, v199, s[6:7]
.LBB0_1102:
	s_or_b64 exec, exec, s[8:9]
	v_cmp_gt_i32_e32 vcc, s14, v200
	v_mov_b32_e32 v5, 0
	s_and_saveexec_b64 s[8:9], vcc
	s_cbranch_execz .LBB0_1104
	global_load_dword v122, v201, s[6:7]
.LBB0_1104:
	s_or_b64 exec, exec, s[8:9]
	v_cmp_gt_i32_e32 vcc, s14, v202
	s_and_saveexec_b64 s[8:9], vcc
	s_cbranch_execz .LBB0_1106
	global_load_dword v123, v199, s[6:7] offset:512
.LBB0_1106:
	s_or_b64 exec, exec, s[8:9]
	v_cmp_gt_i32_e32 vcc, s14, v203
	v_mov_b32_e32 v6, 0
	s_and_saveexec_b64 s[8:9], vcc
	s_cbranch_execz .LBB0_1108
	global_load_dword v124, v201, s[6:7] offset:512
.LBB0_1108:
	s_or_b64 exec, exec, s[8:9]
	s_and_b64 vcc, exec, s[4:5]
	s_cbranch_vccnz .LBB0_1110
	s_mul_i32 s4, s33, 5
	s_add_i32 s4, s4, s2
	s_ashr_i32 s6, s4, 3
	s_cbranch_execz .LBB0_1111
	s_branch .LBB0_1112

; __global__ void __launch_bounds__(NTHREADS, 2) hymba_fwd(Params P) {
;     ...
;             { int R0, C0, R1, C1; g8::stage_rc(tid * 16, R0, C0); g8::stage_rc(tid * 16 + 8192, R1, C1);
; #pragma unroll
;               for (int k = 0; k < 6; ++k) { g8::Unit uk; uk.aux = 0; uk.aux2 = 0; const bool ok = S.next(k, uk);
;                   const int e = uk.aux & 255, r0 = uk.aux >> 8, n = ok ? uk.aux2 : 0; const int* le = (const int*)(ws + WS_LIST) + (ok ? e * 16384 + r0 : 0);
;                   const unsigned a0 = (R0 < n) ? (unsigned)(le[R0] >> 1) : 0u, a1 = (R1 < n) ? (unsigned)(le[R1] >> 1) : 0u, a2 = (128 + R0 < n) ? (unsigned)(le[128 + R0] >> 1) : 0u, a3 = (128 + R1 < n) ? (unsigned)(le[128 + R1] >> 1) : 0u;
;                   tokt[k * 512 + tid] = (u32x2){a0 | (a1 << 16), a2 | (a3 << 16)}; }
.LBB0_1114:
	s_ashr_i32 s6, s7, 8
	s_lshl_b32 s7, s7, 14
	s_and_b32 s7, s7, 0x3fc000
	s_add_i32 s7, s7, s6
	s_and_b64 s[4:5], s[4:5], exec
	s_cselect_b32 s4, s7, 0
	s_ashr_i32 s5, s4, 31
	s_lshl_b64 s[4:5], s[4:5], 2
	s_add_u32 s4, s10, s4
	s_addc_u32 s5, s11, s5
	v_cmp_gt_i32_e32 vcc, s8, v198
	v_mov_b32_e32 v1, 0
	v_mov_b32_e32 v4, 0
	s_and_saveexec_b64 s[6:7], vcc
	s_cbranch_execz .LBB0_1116
	global_load_dword v125, v199, s[4:5]
.LBB0_1116:
	s_or_b64 exec, exec, s[6:7]
	v_cmp_gt_i32_e32 vcc, s8, v200
	v_mov_b32_e32 v5, 0
	s_and_saveexec_b64 s[6:7], vcc
	s_cbranch_execz .LBB0_1118
	global_load_dword v126, v201, s[4:5]
.LBB0_1118:
	s_or_b64 exec, exec, s[6:7]
	v_cmp_gt_i32_e32 vcc, s8, v202
	s_and_saveexec_b64 s[6:7], vcc
	s_cbranch_execz .LBB0_1120
	global_load_dword v127, v199, s[4:5] offset:512
.LBB0_1120:
	s_or_b64 exec, exec, s[6:7]
	v_cmp_gt_i32_e32 vcc, s8, v203
	v_mov_b32_e32 v6, 0
	s_and_saveexec_b64 s[6:7], vcc
	s_cbranch_execz .LBB0_1122
	global_load_dword v128, v201, s[4:5] offset:512
.LBB0_1122:
	s_or_b64 exec, exec, s[6:7]
	v_readfirstlane_b32 s26, v0
	s_and_b64 vcc, exec, s[12:13]
	s_waitcnt vmcnt(0)
	v_ashrrev_i32_e32 v130, 1, v105
	v_lshlrev_b32_e32 v129, 15, v106
	v_and_b32_e32 v129, 0xffff0000, v129
	v_or_b32_e32 v130, v129, v130
	v_ashrrev_i32_e32 v131, 1, v107
	v_lshlrev_b32_e32 v129, 15, v108
	v_and_b32_e32 v129, 0xffff0000, v129
	v_or_b32_e32 v131, v129, v131
	ds_write_b64 v204, v[130:131]
	v_ashrrev_i32_e32 v132, 1, v109
	v_lshlrev_b32_e32 v134, 15, v110
	v_and_b32_e32 v134, 0xffff0000, v134
	v_or_b32_e32 v132, v134, v132
	v_ashrrev_i32_e32 v133, 1, v111
	v_lshlrev_b32_e32 v134, 15, v112
	v_and_b32_e32 v134, 0xffff0000, v134
	v_or_b32_e32 v133, v134, v133
	ds_write_b64 v204, v[132:133] offset:4096
	v_ashrrev_i32_e32 v130, 1, v113
	v_lshlrev_b32_e32 v129, 15, v114
	v_and_b32_e32 v129, 0xffff0000, v129
	v_or_b32_e32 v130, v129, v130
	v_ashrrev_i32_e32 v131, 1, v115
	v_lshlrev_b32_e32 v129, 15, v116
	v_and_b32_e32 v129, 0xffff0000, v129
	v_or_b32_e32 v131, v129, v131
	ds_write_b64 v204, v[130:131] offset:8192
	v_ashrrev_i32_e32 v132, 1, v117
	v_lshlrev_b32_e32 v134, 15, v118
	v_and_b32_e32 v134, 0xffff0000, v134
	v_or_b32_e32 v132, v134, v132
	v_ashrrev_i32_e32 v133, 1, v119
	v_lshlrev_b32_e32 v134, 15, v120
	v_and_b32_e32 v134, 0xffff0000, v134
	v_or_b32_e32 v133, v134, v133
	ds_write_b64 v204, v[132:133] offset:12288
	v_ashrrev_i32_e32 v130, 1, v121
	v_lshlrev_b32_e32 v129, 15, v122
	v_and_b32_e32 v129, 0xffff0000, v129
	v_or_b32_e32 v130, v129, v130
	v_ashrrev_i32_e32 v131, 1, v123
	v_lshlrev_b32_e32 v129, 15, v124
	v_and_b32_e32 v129, 0xffff0000, v129
	v_or_b32_e32 v131, v129, v131
	ds_write_b64 v204, v[130:131] offset:16384
	v_ashrrev_i32_e32 v132, 1, v125
	v_lshlrev_b32_e32 v134, 15, v126
	v_and_b32_e32 v134, 0xffff0000, v134
	v_or_b32_e32 v132, v134, v132
	v_ashrrev_i32_e32 v133, 1, v127
	v_lshlrev_b32_e32 v134, 15, v128
	v_and_b32_e32 v134, 0xffff0000, v134
	v_or_b32_e32 v133, v134, v133
	ds_write_b64 v204, v[132:133] offset:20480
	s_waitcnt lgkmcnt(0)
	s_barrier
	s_cbranch_vccz .LBB0_1124
	s_ashr_i32 s82, s2, 3
	s_mov_b32 s4, s2
	s_cbranch_execz .LBB0_1125
	s_branch .LBB0_1126

; #define LAS __attribute__((address_space(3)))
; __global__ void __launch_bounds__(NTHREADS, 2) hymba_fwd(Params P) {
;     ...
;             LAS u32x2* sl = (LAS u32x2*)(lds + LDS_CONV);
; #pragma unroll
;             for (int k = 0; k < 8; ++k) { g8::Unit uk; uk.pm = 0; const bool ok = S.next(k, uk); const int pmk = ok ? uk.pm : 0;
;                 if (tid < 256) sl[k * 256 + tid] = ((const u32x2*)(ws + WS_SLOT))[pmk * 256 + tid]; }
;             __syncthreads();
.LBB0_1282:
	s_add_i32 s6, 0, 0x20000
	s_movk_i32 s4, 0x100
	s_add_u32 s8, s8, 0x2f63e000
	v_cmp_gt_u32_e64 s[4:5], s4, v0
	v_lshl_add_u32 v1, v0, 3, s6
	s_addc_u32 s9, s9, 0
	s_and_saveexec_b64 s[6:7], s[4:5]
	s_cbranch_execz .LBB0_1284
	v_or_b32_e32 v2, s10, v0
	v_ashrrev_i32_e32 v3, 31, v2
	v_lshl_add_u64 v[2:3], v[2:3], 3, s[8:9]
	global_load_dwordx2 v[4:5], v[2:3], off

; #define LAS __attribute__((address_space(3)))
; __global__ void __launch_bounds__(NTHREADS, 2) hymba_fwd(Params P) {
;     ...
;             LAS u32x2* sl = (LAS u32x2*)(lds + LDS_CONV);
; #pragma unroll
;             for (int k = 0; k < 8; ++k) { g8::Unit uk; uk.pm = 0; const bool ok = S.next(k, uk); const int pmk = ok ? uk.pm : 0;
;                 if (tid < 256) sl[k * 256 + tid] = ((const u32x2*)(ws + WS_SLOT))[pmk * 256 + tid]; }
;             __syncthreads();
.LBB0_1320:
	v_or_b32_e32 v2, s13, v0
	v_ashrrev_i32_e32 v3, 31, v2
	v_lshl_add_u64 v[2:3], v[2:3], 3, s[8:9]
	global_load_dwordx2 v[6:7], v[2:3], off
	s_or_b64 exec, exec, s[10:11]
	s_and_b64 vcc, exec, s[6:7]
	s_cbranch_vccz .LBB0_1290

; #define LAS __attribute__((address_space(3)))
; __global__ void __launch_bounds__(NTHREADS, 2) hymba_fwd(Params P) {
;     ...
;             LAS u32x2* sl = (LAS u32x2*)(lds + LDS_CONV);
; #pragma unroll
;             for (int k = 0; k < 8; ++k) { g8::Unit uk; uk.pm = 0; const bool ok = S.next(k, uk); const int pmk = ok ? uk.pm : 0;
;                 if (tid < 256) sl[k * 256 + tid] = ((const u32x2*)(ws + WS_SLOT))[pmk * 256 + tid]; }
;             __syncthreads();
.LBB0_1323:
	v_or_b32_e32 v2, s13, v0
	v_ashrrev_i32_e32 v3, 31, v2
	v_lshl_add_u64 v[2:3], v[2:3], 3, s[8:9]
	global_load_dwordx2 v[8:9], v[2:3], off
	s_or_b64 exec, exec, s[10:11]
	s_and_b64 vcc, exec, s[6:7]
	s_cbranch_vccz .LBB0_1295

; #define LAS __attribute__((address_space(3)))
; __global__ void __launch_bounds__(NTHREADS, 2) hymba_fwd(Params P) {
;     ...
;             LAS u32x2* sl = (LAS u32x2*)(lds + LDS_CONV);
; #pragma unroll
;             for (int k = 0; k < 8; ++k) { g8::Unit uk; uk.pm = 0; const bool ok = S.next(k, uk); const int pmk = ok ? uk.pm : 0;
;                 if (tid < 256) sl[k * 256 + tid] = ((const u32x2*)(ws + WS_SLOT))[pmk * 256 + tid]; }
;             __syncthreads();
.LBB0_1326:
	v_or_b32_e32 v2, s13, v0
	v_ashrrev_i32_e32 v3, 31, v2
	v_lshl_add_u64 v[2:3], v[2:3], 3, s[8:9]
	global_load_dwordx2 v[10:11], v[2:3], off
	s_or_b64 exec, exec, s[10:11]
	s_and_b64 vcc, exec, s[6:7]
	s_cbranch_vccz .LBB0_1300

; #define LAS __attribute__((address_space(3)))
; __global__ void __launch_bounds__(NTHREADS, 2) hymba_fwd(Params P) {
;     ...
;             LAS u32x2* sl = (LAS u32x2*)(lds + LDS_CONV);
; #pragma unroll
;             for (int k = 0; k < 8; ++k) { g8::Unit uk; uk.pm = 0; const bool ok = S.next(k, uk); const int pmk = ok ? uk.pm : 0;
;                 if (tid < 256) sl[k * 256 + tid] = ((const u32x2*)(ws + WS_SLOT))[pmk * 256 + tid]; }
;             __syncthreads();
.LBB0_1329:
	v_or_b32_e32 v2, s13, v0
	v_ashrrev_i32_e32 v3, 31, v2
	v_lshl_add_u64 v[2:3], v[2:3], 3, s[8:9]
	global_load_dwordx2 v[12:13], v[2:3], off
	s_or_b64 exec, exec, s[10:11]
	s_and_b64 vcc, exec, s[6:7]
	s_cbranch_vccz .LBB0_1305

; #define LAS __attribute__((address_space(3)))
; __global__ void __launch_bounds__(NTHREADS, 2) hymba_fwd(Params P) {
;     ...
;             LAS u32x2* sl = (LAS u32x2*)(lds + LDS_CONV);
; #pragma unroll
;             for (int k = 0; k < 8; ++k) { g8::Unit uk; uk.pm = 0; const bool ok = S.next(k, uk); const int pmk = ok ? uk.pm : 0;
;                 if (tid < 256) sl[k * 256 + tid] = ((const u32x2*)(ws + WS_SLOT))[pmk * 256 + tid]; }
;             __syncthreads();
.LBB0_1332:
	v_or_b32_e32 v2, s13, v0
	v_ashrrev_i32_e32 v3, 31, v2
	v_lshl_add_u64 v[2:3], v[2:3], 3, s[8:9]
	global_load_dwordx2 v[14:15], v[2:3], off
	s_or_b64 exec, exec, s[10:11]
	s_and_b64 vcc, exec, s[6:7]
	s_cbranch_vccz .LBB0_1310

; #define LAS __attribute__((address_space(3)))
; __global__ void __launch_bounds__(NTHREADS, 2) hymba_fwd(Params P) {
;     ...
;             LAS u32x2* sl = (LAS u32x2*)(lds + LDS_CONV);
; #pragma unroll
;             for (int k = 0; k < 8; ++k) { g8::Unit uk; uk.pm = 0; const bool ok = S.next(k, uk); const int pmk = ok ? uk.pm : 0;
;                 if (tid < 256) sl[k * 256 + tid] = ((const u32x2*)(ws + WS_SLOT))[pmk * 256 + tid]; }
;             __syncthreads();
.LBB0_1335:
	v_or_b32_e32 v2, s13, v0
	v_ashrrev_i32_e32 v3, 31, v2
	v_lshl_add_u64 v[2:3], v[2:3], 3, s[8:9]
	global_load_dwordx2 v[16:17], v[2:3], off
	s_or_b64 exec, exec, s[10:11]
	s_and_b64 vcc, exec, s[6:7]
	s_cbranch_vccz .LBB0_1315

; #define LAS __attribute__((address_space(3)))
; __global__ void __launch_bounds__(NTHREADS, 2) hymba_fwd(Params P) {
;     ...
;             LAS u32x2* sl = (LAS u32x2*)(lds + LDS_CONV);
; #pragma unroll
;             for (int k = 0; k < 8; ++k) { g8::Unit uk; uk.pm = 0; const bool ok = S.next(k, uk); const int pmk = ok ? uk.pm : 0;
;                 if (tid < 256) sl[k * 256 + tid] = ((const u32x2*)(ws + WS_SLOT))[pmk * 256 + tid]; }
;             __syncthreads();
.LBB0_1338:
	v_or_b32_e32 v2, s11, v0
	v_ashrrev_i32_e32 v3, 31, v2
	v_lshl_add_u64 v[2:3], v[2:3], 3, s[8:9]
	global_load_dwordx2 v[18:19], v[2:3], off
.LBB0_1339:
	s_or_b64 exec, exec, s[6:7]
	s_and_saveexec_b64 s[10:11], s[4:5]
	s_waitcnt vmcnt(0)
	ds_write_b64 v1, v[4:5]
	ds_write_b64 v1, v[6:7] offset:2048
	ds_write_b64 v1, v[8:9] offset:4096
	ds_write_b64 v1, v[10:11] offset:6144
	ds_write_b64 v1, v[12:13] offset:8192
	ds_write_b64 v1, v[14:15] offset:10240
	ds_write_b64 v1, v[16:17] offset:12288
	ds_write_b64 v1, v[18:19] offset:14336
	s_or_b64 exec, exec, s[10:11]
	v_readfirstlane_b32 s14, v0
	s_and_b64 vcc, exec, s[0:1]
	s_waitcnt vmcnt(0) lgkmcnt(0)
	s_barrier
	s_cbranch_vccz .LBB0_1413
	s_ashr_i32 s70, s2, 3
	s_mov_b32 s4, s2
	s_cbranch_execnz .LBB0_1342
